# t13 without E2 + no 16-register score copies: second half accumulates chain B in v[66:81], consumes first-half block in place, V fragments in v[154:169]
# speedup vs baseline: 1.0057x; 1.0057x over previous
; template <bool FIRST> DEVI bool partialSM(f32x16& p0, f32x16& p1, float& m_reg, float& alpha) {
;     float pmax = p0[0];
; #pragma unroll
;     for (int r = 1; r < 16; ++r) pmax = fmaxf(pmax, p0[r]);
; #pragma unroll
;     for (int r = 0; r < 16; ++r) pmax = fmaxf(pmax, p1[r]);
;     { auto rr = __builtin_amdgcn_permlane32_swap(__float_as_uint(pmax), __float_as_uint(pmax), false, false);
;       pmax = fmaxf(__uint_as_float(rr[0]), __uint_as_float(rr[1])); }
;     if (FIRST) { m_reg = pmax; alpha = 1.f;
; #pragma unroll
;         for (int r = 0; r < 16; ++r) { p0[r] = __builtin_amdgcn_exp2f(p0[r] - pmax); p1[r] = p1[r] - pmax; }
;         return false;
;     } else if (__builtin_expect(__all(pmax <= ATT_THR), 1)) { alpha = 1.f;
; #pragma unroll
;         for (int r = 0; r < 16; ++r) p0[r] = __builtin_amdgcn_exp2f(p0[r]);
;         return false;
;     } else { const float d = fmaxf(pmax, 0.f); alpha = __builtin_amdgcn_exp2f(-d); m_reg += d;
; #pragma unroll
;         for (int r = 0; r < 16; ++r) { p0[r] = __builtin_amdgcn_exp2f(p0[r] - d); p1[r] = p1[r] - d; }
;         return true;
;     }
; }
; DEVI void finishSM(f32x16& p0, f32x16& p1, float alpha, float& l_reg, bf16x8& pa0, bf16x8& pa1, bf16x8& pa2, bf16x8& pa3) {
; #pragma unroll
;     for (int r = 0; r < 16; ++r) p1[r] = __builtin_amdgcn_exp2f(p1[r]);
;     f32x2 s2 = (f32x2){p0[0], p0[1]} + (f32x2){p1[0], p1[1]};
; #pragma unroll
;     for (int r = 2; r < 16; r += 2) s2 += (f32x2){p0[r], p0[r + 1]} + (f32x2){p1[r], p1[r + 1]};
;     float ps = s2[0] + s2[1];
;     { auto rr = __builtin_amdgcn_permlane32_swap(__float_as_uint(ps), __float_as_uint(ps), false, false);
;       ps = __uint_as_float(rr[0]) + __uint_as_float(rr[1]); }
;     l_reg = l_reg * alpha + ps;
;     ...
;     PK4(p0, 0, pa0); PK4(p0, 8, pa1); PK4(p1, 0, pa2); PK4(p1, 8, pa3);
;     ...
; }
; DEVI void qkt(f32x16& p0, f32x16& p1, const char* Kb, const bf16x8 (&qr)[6], int r32, int hi, const f32x16& cinit) {
; #pragma unroll
;     for (int d0 = 0; d0 < 6; ++d0) { const int cb = (d0 * 16 + hi * 8) * 2;
;         const bf16x8 k0 = *(const bf16x8*)(Kb + KSWZ(r32, cb)), k1 = *(const bf16x8*)(Kb + KSWZ(32 + r32, cb));
;         p0 = __builtin_amdgcn_mfma_f32_32x32x16_bf16(k0, qr[d0], d0 == 0 ? cinit : p0, 0, 0, 0);
;         p1 = __builtin_amdgcn_mfma_f32_32x32x16_bf16(k1, qr[d0], d0 == 0 ? cinit : p1, 0, 0, 0); }
; }
.LBB0_696:
	v_add_u32_e32 v174, s98, v204
	v_exp_f32_e32 v66, v66
	v_exp_f32_e32 v67, v67
	s_waitcnt lgkmcnt(1)
	v_mfma_f32_32x32x16_bf16 v[98:113], v[82:85], v[150:153], v[34:49]
	v_add_u32_e32 v82, s98, v184
	v_add_u32_e32 v83, s98, v185
	ds_read_b128 v[208:211], v82 offset:12288
	ds_read_b128 v[212:215], v82 offset:18432
	ds_read_b128 v[216:219], v83 offset:12288
	ds_read_b128 v[220:223], v83 offset:18432
	v_exp_f32_e32 v68, v68
	v_exp_f32_e32 v69, v69
	v_exp_f32_e32 v70, v70
	v_exp_f32_e32 v71, v71
	s_waitcnt lgkmcnt(4)
	v_mfma_f32_32x32x16_bf16 v[82:97], v[124:127], v[150:153], v[34:49]
	ds_read_b128 v[124:127], v174 offset:12288
	ds_read_b128 v[224:227], v174 offset:18432
	v_exp_f32_e32 v72, v72
	v_exp_f32_e32 v73, v73
	v_exp_f32_e32 v74, v74
	v_exp_f32_e32 v75, v75
	v_exp_f32_e32 v76, v76
	v_exp_f32_e32 v77, v77
	s_waitcnt lgkmcnt(5)
	v_mfma_f32_32x32x16_bf16 v[98:113], v[208:211], v[138:141], v[98:113]
	v_add_u32_e32 v174, s98, v205
	v_exp_f32_e32 v78, v78
	v_exp_f32_e32 v79, v79
	ds_read_b128 v[228:231], v174 offset:12288
	ds_read_b128 v[232:235], v174 offset:18432
	v_exp_f32_e32 v80, v80
	v_exp_f32_e32 v81, v81
	v_add_u32_e32 v174, s98, v206
	s_waitcnt lgkmcnt(6)
	v_mfma_f32_32x32x16_bf16 v[82:97], v[212:215], v[138:141], v[82:97]
	v_add_f32_e64 v212, v50, v66
	v_add_f32_e64 v213, v51, v67
	v_add_f32_e64 v214, v52, v68
	v_add_f32_e64 v215, v53, v69
	v_lshl_add_u32 v202, s89, 14, v115
	v_add_f32_e32 v212, v214, v212
	v_add_f32_e32 v213, v215, v213
	v_add_f32_e32 v214, v54, v70
	v_add_f32_e32 v215, v55, v71
	ds_read_b128 v[208:211], v174 offset:12288
	ds_read_b128 v[236:239], v174 offset:18432
	v_add_f32_e32 v212, v214, v212
	v_add_f32_e32 v213, v215, v213
	s_waitcnt lgkmcnt(7)
	v_mfma_f32_32x32x16_bf16 v[98:113], v[216:219], v[134:137], v[98:113]
	v_add_f32_e64 v214, v56, v72
	v_add_f32_e64 v215, v57, v73
	v_cvt_pk_bf16_f32 v50, v50, v51
	v_cvt_pk_bf16_f32 v51, v52, v53
	v_cvt_pk_bf16_f32 v52, v54, v55
	v_cvt_pk_bf16_f32 v53, v56, v57
	v_cvt_pk_bf16_f32 v54, v58, v59
	v_add_f32_e64 v212, v214, v212
	v_add_f32_e64 v213, v215, v213
	s_waitcnt lgkmcnt(6)
	v_mfma_f32_32x32x16_bf16 v[82:97], v[220:223], v[134:137], v[82:97]
	v_add_f32_e64 v214, v58, v74
	v_add_f32_e64 v215, v59, v75
	v_cvt_pk_bf16_f32 v55, v60, v61
	v_cvt_pk_bf16_f32 v56, v62, v63
	v_cvt_pk_bf16_f32 v57, v64, v65
	v_cvt_pk_bf16_f32 v58, v66, v67
	v_cvt_pk_bf16_f32 v59, v68, v69
	v_add_f32_e64 v212, v214, v212
	v_add_f32_e64 v213, v215, v213
	s_waitcnt lgkmcnt(5)
	v_mfma_f32_32x32x16_bf16 v[98:113], v[124:127], v[130:133], v[98:113]
	v_add_f32_e64 v214, v60, v76
	v_add_f32_e64 v215, v61, v77
	v_add_f32_e64 v126, v62, v78
	v_add_f32_e64 v127, v63, v79
	v_add_f32_e64 v124, v214, v212
	v_add_f32_e64 v125, v215, v213
	v_cvt_pk_bf16_f32 v60, v70, v71
	v_cvt_pk_bf16_f32 v61, v72, v73
	v_cvt_pk_bf16_f32 v62, v74, v75
	v_cvt_pk_bf16_f32 v63, v76, v77
	s_waitcnt lgkmcnt(4)
	v_mfma_f32_32x32x16_bf16 v[82:97], v[224:227], v[130:133], v[82:97]
	v_add_f32_e64 v124, v126, v124
	v_add_f32_e64 v125, v127, v125
	v_add_f32_e64 v126, v64, v80
	v_add_f32_e64 v127, v65, v81
	v_cvt_pk_bf16_f32 v64, v78, v79
	v_cvt_pk_bf16_f32 v65, v80, v81
	ds_read_b64_tr_b16 v[66:67], v202 offset:0
	ds_read_b64_tr_b16 v[68:69], v202 offset:0x400
	ds_read_b64_tr_b16 v[70:71], v202 offset:0x800
	s_waitcnt lgkmcnt(6)
	v_mfma_f32_32x32x16_bf16 v[98:113], v[228:231], v[146:149], v[98:113]
	ds_read_b64_tr_b16 v[72:73], v202 offset:0xc00
	ds_read_b64_tr_b16 v[74:75], v202 offset:0x1000
	ds_read_b64_tr_b16 v[76:77], v202 offset:0x1400
	ds_read_b64_tr_b16 v[78:79], v202 offset:0x1800
	ds_read_b64_tr_b16 v[80:81], v202 offset:0x1c00
	v_add_f32_e64 v124, v126, v124
	v_add_f32_e64 v125, v127, v125
	s_waitcnt lgkmcnt(10)
	v_mfma_f32_32x32x16_bf16 v[82:97], v[232:235], v[146:149], v[82:97]
	v_add_f32_e32 v124, v124, v125
	s_nop 0
	v_mov_b32_e32 v125, v124
	s_nop 1
	v_permlane32_swap_b32_e32 v124, v125
	s_waitcnt lgkmcnt(9)
	v_mfma_f32_32x32x16_bf16 v[98:113], v[208:211], v[142:145], v[98:113]
	ds_read_b64_tr_b16 v[208:209], v202 offset:0x200
	ds_read_b64_tr_b16 v[210:211], v202 offset:0x600
	ds_read_b64_tr_b16 v[212:213], v202 offset:0xa00
	ds_read_b64_tr_b16 v[214:215], v202 offset:0xe00
	ds_read_b64_tr_b16 v[216:217], v202 offset:0x1200
	ds_read_b64_tr_b16 v[218:219], v202 offset:0x1600
	ds_read_b64_tr_b16 v[220:221], v202 offset:0x1a00
	s_waitcnt lgkmcnt(15)
	v_mfma_f32_32x32x16_bf16 v[82:97], v[236:239], v[142:145], v[82:97]
	ds_read_b64_tr_b16 v[222:223], v202 offset:0x1e00
	s_waitcnt lgkmcnt(14)
	v_mfma_f32_32x32x16_bf16 v[18:33], v[50:53], v[66:69], v[18:33]
	s_waitcnt lgkmcnt(6)
	v_mfma_f32_32x32x16_bf16 v[2:17], v[50:53], v[208:211], v[2:17]
	s_nop 8
	v_max_f32_e32 v249, v99, v99
	v_max_f32_e32 v250, v98, v98
	v_max_f32_e32 v249, v250, v249
	v_max3_f32 v249, v249, v100, v101
	v_max3_f32 v249, v249, v102, v103
	v_max3_f32 v251, v249, v104, v105
	v_max3_f32 v251, v251, v106, v107
	v_exp_f32_e32 v50, v98
	v_exp_f32_e32 v51, v99
	v_exp_f32_e32 v52, v100
	v_exp_f32_e32 v53, v101
	v_mfma_f32_32x32x16_bf16 v[18:33], v[54:57], v[70:73], v[18:33]
	s_waitcnt lgkmcnt(4)
	v_mfma_f32_32x32x16_bf16 v[2:17], v[54:57], v[212:215], v[2:17]
	v_max3_f32 v251, v251, v108, v109
	v_max3_f32 v251, v251, v110, v111
	v_max3_f32 v251, v251, v112, v113
	v_max3_f32 v251, v251, v82, v83
	v_max3_f32 v251, v251, v84, v85
	v_max3_f32 v251, v251, v86, v87
	v_max3_f32 v251, v251, v88, v89
	v_exp_f32_e32 v54, v102
	v_exp_f32_e32 v55, v103
	v_exp_f32_e32 v56, v104
	v_exp_f32_e32 v57, v105
	v_mfma_f32_32x32x16_bf16 v[18:33], v[58:61], v[74:77], v[18:33]
	s_waitcnt lgkmcnt(2)
	v_mfma_f32_32x32x16_bf16 v[2:17], v[58:61], v[216:219], v[2:17]
	v_max3_f32 v251, v251, v90, v91
	v_max3_f32 v251, v251, v92, v93
	v_max3_f32 v251, v251, v94, v95
	v_max3_f32 v251, v251, v96, v97
	v_mov_b32_e32 v252, v251
	s_nop 1
	v_permlane32_swap_b32_e32 v251, v252
	v_exp_f32_e32 v58, v106
	v_exp_f32_e32 v59, v107
	v_exp_f32_e32 v60, v108
	v_exp_f32_e32 v61, v109
	v_mfma_f32_32x32x16_bf16 v[18:33], v[62:65], v[78:81], v[18:33]
	s_waitcnt lgkmcnt(0)
	v_mfma_f32_32x32x16_bf16 v[2:17], v[62:65], v[220:223], v[2:17]
	v_exp_f32_e32 v62, v110
	v_exp_f32_e32 v63, v111
	v_exp_f32_e32 v64, v112
	v_exp_f32_e32 v65, v113
	v_max_f32_e32 v252, v252, v252
	v_max_f32_e32 v251, v251, v251
	v_max_f32_e32 v126, v251, v252
	v_cmp_ge_f32_e32 vcc, s79, v126
	s_cmp_lg_u64 vcc, exec
	s_cselect_b64 s[6:7], -1, 0
	s_cbranch_scc1 .LBB0_705
	v_mov_b32_e32 v208, 1.0
	v_mov_b32_e32 v209, v203
	s_branch .LBB0_699

; #define VM0() asm volatile("s_waitcnt vmcnt(0)" ::: "memory")
; DEVI void attn_unit8(const Params& p, char* smem, int unit, int l, int& cvs  , CvRun& crun) {
;     ...
;         if (cvr.live) asm volatile("s_waitcnt vmcnt(2)" ::: "memory"); else VM0();
;         __syncthreads();
;         if (T + 2 < NTILE) B_DMA(T + 2, s2);
;         qkt(pA0, pA1, K_lds + s1 * 24576, qr, r32, hi, cinit);
.LBB0_702:
	s_mul_i32 s98, s2, 0x6000
	s_add_i32 s98, s96, s98
	s_lshl_b32 s99, s2, 14
	s_add_i32 s99, s97, s99
	s_mul_i32 s6, s61, 0x6000
	s_add_i32 s6, s6, 0
	v_add_u32_e32 v249, s6, v129
	v_lshl_add_u64 v[250:251], v[118:119], 0, s[12:13]
	s_mov_b32 m0, s98
	s_barrier
; template <bool FIRST> DEVI bool partialSM(f32x16& p0, f32x16& p1, float& m_reg, float& alpha) {
;     float pmax = p0[0];
; #pragma unroll
;     for (int r = 1; r < 16; ++r) pmax = fmaxf(pmax, p0[r]);
; #pragma unroll
;     for (int r = 0; r < 16; ++r) pmax = fmaxf(pmax, p1[r]);
;     { auto rr = __builtin_amdgcn_permlane32_swap(__float_as_uint(pmax), __float_as_uint(pmax), false, false);
;       pmax = fmaxf(__uint_as_float(rr[0]), __uint_as_float(rr[1])); }
;     if (FIRST) { m_reg = pmax; alpha = 1.f;
; #pragma unroll
;         for (int r = 0; r < 16; ++r) { p0[r] = __builtin_amdgcn_exp2f(p0[r] - pmax); p1[r] = p1[r] - pmax; }
;         return false;
;     } else if (__builtin_expect(__all(pmax <= ATT_THR), 1)) { alpha = 1.f;
; #pragma unroll
;         for (int r = 0; r < 16; ++r) p0[r] = __builtin_amdgcn_exp2f(p0[r]);
;         return false;
;     } else { const float d = fmaxf(pmax, 0.f); alpha = __builtin_amdgcn_exp2f(-d); m_reg += d;
; #pragma unroll
;         for (int r = 0; r < 16; ++r) { p0[r] = __builtin_amdgcn_exp2f(p0[r] - d); p1[r] = p1[r] - d; }
;         return true;
;     }
; }
; DEVI void finishSM(f32x16& p0, f32x16& p1, float alpha, float& l_reg, bf16x8& pa0, bf16x8& pa1, bf16x8& pa2, bf16x8& pa3) {
; #pragma unroll
;     for (int r = 0; r < 16; ++r) p1[r] = __builtin_amdgcn_exp2f(p1[r]);
;     f32x2 s2 = (f32x2){p0[0], p0[1]} + (f32x2){p1[0], p1[1]};
; #pragma unroll
;     for (int r = 2; r < 16; r += 2) s2 += (f32x2){p0[r], p0[r + 1]} + (f32x2){p1[r], p1[r + 1]};
;     float ps = s2[0] + s2[1];
;     { auto rr = __builtin_amdgcn_permlane32_swap(__float_as_uint(ps), __float_as_uint(ps), false, false);
;       ps = __uint_as_float(rr[0]) + __uint_as_float(rr[1]); }
;     l_reg = l_reg * alpha + ps;
;     ...
;     PK4(p0, 0, pa0); PK4(p0, 8, pa1); PK4(p1, 0, pa2); PK4(p1, 8, pa3);
;     ...
; }
; DEVI void qkt(f32x16& p0, f32x16& p1, const char* Kb, const bf16x8 (&qr)[6], int r32, int hi, const f32x16& cinit) {
; #pragma unroll
;     for (int d0 = 0; d0 < 6; ++d0) { const int cb = (d0 * 16 + hi * 8) * 2;
;         const bf16x8 k0 = *(const bf16x8*)(Kb + KSWZ(r32, cb)), k1 = *(const bf16x8*)(Kb + KSWZ(32 + r32, cb));
;         p0 = __builtin_amdgcn_mfma_f32_32x32x16_bf16(k0, qr[d0], d0 == 0 ? cinit : p0, 0, 0, 0);
;         p1 = __builtin_amdgcn_mfma_f32_32x32x16_bf16(k1, qr[d0], d0 == 0 ? cinit : p1, 0, 0, 0); }
; }
	ds_read_b128 v[234:237], v249
	ds_read_b128 v[210:213], v249 offset:6144
	global_load_lds_dwordx4 v[250:251], off
	v_exp_f32_e32 v82, v82
	s_waitcnt lgkmcnt(1)
	v_mfma_f32_32x32x16_bf16 v[98:113], v[234:237], v[150:153], v[34:49]
	v_add_u32_e32 v126, s6, v184
	v_lshl_add_u64 v[250:251], v[120:121], 0, s[12:13]
	s_add_i32 m0, s98, 0x2000
	v_exp_f32_e32 v83, v83
	v_exp_f32_e32 v84, v84
	global_load_lds_dwordx4 v[250:251], off
	v_exp_f32_e32 v85, v85
	v_exp_f32_e32 v86, v86
	v_exp_f32_e32 v87, v87
	v_exp_f32_e32 v88, v88
	s_waitcnt lgkmcnt(0)
	v_mfma_f32_32x32x16_bf16 v[66:81], v[210:213], v[150:153], v[34:49]
	ds_read_b128 v[210:213], v126
	ds_read_b128 v[214:217], v126 offset:6144
	v_add_u32_e32 v126, s6, v185
	v_lshl_add_u64 v[250:251], v[122:123], 0, s[12:13]
	s_add_i32 m0, s98, 0x4000
	v_exp_f32_e32 v89, v89
	v_exp_f32_e32 v90, v90
	global_load_lds_dwordx4 v[250:251], off
	v_exp_f32_e32 v91, v91
	v_exp_f32_e32 v92, v92
	v_exp_f32_e32 v93, v93
	s_waitcnt lgkmcnt(1)
	v_mfma_f32_32x32x16_bf16 v[98:113], v[210:213], v[138:141], v[98:113]
	s_mov_b32 m0, s99
	v_exp_f32_e32 v94, v94
	v_exp_f32_e32 v95, v95
	v_lshl_add_u64 v[250:251], v[116:117], 0, s[40:41]
	global_load_lds_dwordx4 v[116:117], off
	s_add_i32 m0, s99, 0x2000
	v_exp_f32_e32 v96, v96
	v_exp_f32_e32 v97, v97
	v_add_u32_e32 v174, 0x2000, v202
	global_load_lds_dwordx4 v[250:251], off
	s_waitcnt lgkmcnt(0)
	v_mfma_f32_32x32x16_bf16 v[66:81], v[214:217], v[138:141], v[66:81]
	ds_read_b128 v[210:213], v126
	ds_read_b128 v[214:217], v126 offset:6144
	v_add_u32_e32 v126, s6, v204
	s_waitcnt lgkmcnt(1)
	v_mfma_f32_32x32x16_bf16 v[98:113], v[210:213], v[134:137], v[98:113]
	ds_read_b128 v[210:213], v126
	ds_read_b128 v[218:221], v126 offset:6144
	v_add_u32_e32 v126, s6, v205
	s_waitcnt lgkmcnt(2)
	v_mfma_f32_32x32x16_bf16 v[66:81], v[214:217], v[134:137], v[66:81]
	ds_read_b128 v[214:217], v126
	ds_read_b128 v[222:225], v126 offset:6144
	v_add_u32_e32 v126, s6, v206
	ds_read_b128 v[226:229], v126
	ds_read_b128 v[230:233], v126 offset:6144
	v_add_f32_e32 v126, v50, v82
	v_add_f32_e32 v127, v51, v83
	v_cvt_pk_bf16_f32 v50, v50, v51
	v_cvt_pk_bf16_f32 v51, v52, v53
	s_waitcnt lgkmcnt(5)
	v_mfma_f32_32x32x16_bf16 v[98:113], v[210:213], v[130:133], v[98:113]
	v_add_f32_e64 v210, v52, v84
	v_add_f32_e64 v211, v53, v85
	v_cvt_pk_bf16_f32 v52, v54, v55
	v_cvt_pk_bf16_f32 v53, v56, v57
	v_add_f32_e64 v126, v210, v126
	v_add_f32_e64 v127, v211, v127
	v_add_f32_e64 v210, v54, v86
	v_add_f32_e64 v211, v55, v87
	v_cvt_pk_bf16_f32 v54, v58, v59
	s_waitcnt lgkmcnt(4)
	v_mfma_f32_32x32x16_bf16 v[66:81], v[218:221], v[130:133], v[66:81]
	v_add_f32_e64 v126, v210, v126
	v_add_f32_e64 v127, v211, v127
	v_add_f32_e64 v210, v56, v88
	v_add_f32_e64 v211, v57, v89
	v_cvt_pk_bf16_f32 v55, v60, v61
	v_cvt_pk_bf16_f32 v56, v62, v63
	v_cvt_pk_bf16_f32 v57, v64, v65
	v_add_f32_e64 v126, v210, v126
	v_add_f32_e64 v127, v211, v127
	v_add_f32_e32 v210, v58, v90
	v_add_f32_e32 v211, v59, v91
	v_cvt_pk_bf16_f32 v58, v82, v83
	v_cvt_pk_bf16_f32 v59, v84, v85
	s_waitcnt lgkmcnt(3)
	v_mfma_f32_32x32x16_bf16 v[98:113], v[214:217], v[146:149], v[98:113]
	v_add_f32_e64 v126, v210, v126
	v_add_f32_e64 v127, v211, v127
	v_add_f32_e64 v210, v60, v92
	v_add_f32_e64 v211, v61, v93
	v_cvt_pk_bf16_f32 v60, v86, v87
	v_cvt_pk_bf16_f32 v61, v88, v89
	v_add_f32_e64 v126, v210, v126
	v_add_f32_e64 v127, v211, v127
	v_add_f32_e32 v210, v62, v94
	v_add_f32_e32 v211, v63, v95
	v_cvt_pk_bf16_f32 v62, v90, v91
	v_cvt_pk_bf16_f32 v63, v92, v93
	s_waitcnt lgkmcnt(2)
	v_mfma_f32_32x32x16_bf16 v[66:81], v[222:225], v[146:149], v[66:81]
	v_add_f32_e64 v126, v210, v126
	v_add_f32_e64 v127, v211, v127
	v_add_f32_e64 v210, v64, v96
	v_add_f32_e64 v211, v65, v97
	v_cvt_pk_bf16_f32 v64, v94, v95
	v_cvt_pk_bf16_f32 v65, v96, v97
	ds_read_b64_tr_b16 v[154:155], v174 offset:0
	ds_read_b64_tr_b16 v[156:157], v174 offset:0x400
	ds_read_b64_tr_b16 v[158:159], v174 offset:0x800
	ds_read_b64_tr_b16 v[160:161], v174 offset:0xc00
	ds_read_b64_tr_b16 v[162:163], v174 offset:0x1000
	ds_read_b64_tr_b16 v[164:165], v174 offset:0x1400
	ds_read_b64_tr_b16 v[166:167], v174 offset:0x1800
	ds_read_b64_tr_b16 v[168:169], v174 offset:0x1c00
	v_add_f32_e64 v126, v210, v126
	v_add_f32_e64 v127, v211, v127
	ds_read_b64_tr_b16 v[210:211], v174 offset:0x200
	ds_read_b64_tr_b16 v[212:213], v174 offset:0x600
	ds_read_b64_tr_b16 v[214:215], v174 offset:0xa00
	s_waitcnt lgkmcnt(12)
	v_mfma_f32_32x32x16_bf16 v[98:113], v[226:229], v[142:145], v[98:113]
	ds_read_b64_tr_b16 v[216:217], v174 offset:0xe00
	ds_read_b64_tr_b16 v[218:219], v174 offset:0x1200
	ds_read_b64_tr_b16 v[220:221], v174 offset:0x1600
	ds_read_b64_tr_b16 v[222:223], v174 offset:0x1a00
	ds_read_b64_tr_b16 v[224:225], v174 offset:0x1e00
	v_add_f32_e32 v126, v126, v127
	s_waitcnt lgkmcnt(15)
	v_mfma_f32_32x32x16_bf16 v[66:81], v[230:233], v[142:145], v[66:81]
	v_mov_b32_e32 v127, v126
	s_nop 1
	v_permlane32_swap_b32_e32 v126, v127
	s_waitcnt lgkmcnt(14)
	v_mfma_f32_32x32x16_bf16 v[18:33], v[50:53], v[154:157], v[18:33]
	s_waitcnt lgkmcnt(6)
	v_mfma_f32_32x32x16_bf16 v[2:17], v[50:53], v[210:213], v[2:17]
	s_nop 4
	v_max_f32_e32 v249, v99, v99
	v_max_f32_e32 v250, v98, v98
	v_max_f32_e32 v249, v250, v249
	v_max3_f32 v249, v249, v100, v101
	v_max3_f32 v249, v249, v102, v103
	v_max3_f32 v251, v249, v104, v105
	v_max3_f32 v251, v251, v106, v107
	v_exp_f32_e32 v50, v98
	v_exp_f32_e32 v51, v99
	v_exp_f32_e32 v52, v100
	v_exp_f32_e32 v53, v101
	v_mfma_f32_32x32x16_bf16 v[18:33], v[54:57], v[158:161], v[18:33]
	s_waitcnt lgkmcnt(4)
	v_mfma_f32_32x32x16_bf16 v[2:17], v[54:57], v[214:217], v[2:17]
	v_max3_f32 v251, v251, v108, v109
	v_max3_f32 v251, v251, v110, v111
	v_max3_f32 v251, v251, v112, v113
	v_max3_f32 v251, v251, v66, v67
	v_max3_f32 v251, v251, v68, v69
	v_max3_f32 v251, v251, v70, v71
	v_max3_f32 v251, v251, v72, v73
	v_exp_f32_e32 v54, v102
	v_exp_f32_e32 v55, v103
	v_exp_f32_e32 v56, v104
	v_exp_f32_e32 v57, v105
	v_mfma_f32_32x32x16_bf16 v[18:33], v[58:61], v[162:165], v[18:33]
	s_waitcnt lgkmcnt(2)
	v_mfma_f32_32x32x16_bf16 v[2:17], v[58:61], v[218:221], v[2:17]
	v_max3_f32 v251, v251, v74, v75
	v_max3_f32 v251, v251, v76, v77
	v_max3_f32 v251, v251, v78, v79
	v_max3_f32 v251, v251, v80, v81
	v_mov_b32_e32 v252, v251
	s_nop 1
	v_permlane32_swap_b32_e32 v251, v252
	v_exp_f32_e32 v58, v106
	v_exp_f32_e32 v59, v107
	v_exp_f32_e32 v60, v108
	v_exp_f32_e32 v61, v109
	v_mfma_f32_32x32x16_bf16 v[18:33], v[62:65], v[166:169], v[18:33]
	s_waitcnt lgkmcnt(0)
	v_mfma_f32_32x32x16_bf16 v[2:17], v[62:65], v[222:225], v[2:17]
	v_exp_f32_e32 v62, v110
	v_exp_f32_e32 v63, v111
	v_exp_f32_e32 v64, v112
	v_exp_f32_e32 v65, v113
	v_max_f32_e32 v252, v252, v252
	v_max_f32_e32 v251, v251, v251
	v_max_f32_e32 v174, v251, v252
	v_cmp_ge_f32_e32 vcc, s79, v174
	s_cmp_lg_u64 vcc, exec
	s_cselect_b64 s[6:7], -1, 0
	s_cbranch_scc1 .LBB0_711
	v_mov_b32_e32 v202, 1.0
	v_mov_b32_e32 v203, v209
	s_branch .LBB0_716

; template <bool FIRST> DEVI bool partialSM(f32x16& p0, f32x16& p1, float& m_reg, float& alpha) {
;     ...
;     } else { const float d = fmaxf(pmax, 0.f); alpha = __builtin_amdgcn_exp2f(-d); m_reg += d;
; #pragma unroll
;         for (int r = 0; r < 16; ++r) { p0[r] = __builtin_amdgcn_exp2f(p0[r] - d); p1[r] = p1[r] - d; }
;         return true;
;     }
.LBB0_705:
	v_max_f32_e32 v50, v126, v126
	v_max_f32_e32 v66, 0, v50
	v_sub_f32_e32 v50, v98, v66
	v_sub_f32_e32 v51, v99, v66
	v_sub_f32_e32 v52, v100, v66
	v_sub_f32_e32 v53, v101, v66
	v_sub_f32_e32 v54, v102, v66
	v_sub_f32_e32 v55, v103, v66
	v_sub_f32_e32 v56, v104, v66
	v_sub_f32_e32 v57, v105, v66
	v_sub_f32_e32 v58, v106, v66
	v_sub_f32_e32 v59, v107, v66
	v_sub_f32_e32 v60, v108, v66
	v_sub_f32_e32 v61, v109, v66
	v_sub_f32_e32 v62, v110, v66
	v_sub_f32_e32 v63, v111, v66
	v_sub_f32_e32 v64, v112, v66
	v_sub_f32_e32 v65, v113, v66
	v_exp_f32_e64 v208, -v66
	v_add_f32_e32 v209, v203, v66
	v_exp_f32_e32 v50, v50
	v_exp_f32_e32 v51, v51
	v_exp_f32_e32 v52, v52
	v_exp_f32_e32 v53, v53
	v_exp_f32_e32 v54, v54
	v_exp_f32_e32 v55, v55
	v_exp_f32_e32 v56, v56
	v_exp_f32_e32 v57, v57
	v_exp_f32_e32 v58, v58
	v_exp_f32_e32 v59, v59
	v_exp_f32_e32 v60, v60
	v_exp_f32_e32 v61, v61
	v_exp_f32_e32 v62, v62
	v_exp_f32_e32 v63, v63
	v_exp_f32_e32 v64, v64
	v_exp_f32_e32 v65, v65
	v_sub_f32_e32 v97, v97, v66
	v_sub_f32_e32 v96, v96, v66
	v_sub_f32_e32 v95, v95, v66
	v_sub_f32_e32 v94, v94, v66
	v_sub_f32_e32 v93, v93, v66
	v_sub_f32_e32 v92, v92, v66
	v_sub_f32_e32 v91, v91, v66
	v_sub_f32_e32 v90, v90, v66
	v_sub_f32_e32 v89, v89, v66
	v_sub_f32_e32 v88, v88, v66
	v_sub_f32_e32 v87, v87, v66
	v_sub_f32_e32 v86, v86, v66
	v_sub_f32_e32 v85, v85, v66
	v_sub_f32_e32 v84, v84, v66
	v_sub_f32_e32 v83, v83, v66
	v_sub_f32_e32 v82, v82, v66
	s_cbranch_execnz .LBB0_698

; DEVI unsigned cvt_pk_bf16(float lo, float hi) { unsigned r; asm volatile("v_cvt_pk_bf16_f32 %0, %1, %2" : "=v"(r) : "v"(lo), "v"(hi)); return r; }
; template <bool FIRST> DEVI bool partialSM(f32x16& p0, f32x16& p1, float& m_reg, float& alpha) {
;     ...
;     } else { const float d = fmaxf(pmax, 0.f); alpha = __builtin_amdgcn_exp2f(-d); m_reg += d;
; #pragma unroll
;         for (int r = 0; r < 16; ++r) { p0[r] = __builtin_amdgcn_exp2f(p0[r] - d); p1[r] = p1[r] - d; }
;         return true;
;     }
; DEVI void cv_finish(char* img  , int lane, const CvRegs& R) {
;     if (!R.live) return;
;     const int n4 = (lane & 7) * 4, kq = lane >> 3;
;     const float sc = R.c.perm ? 16.f : 1.f;
; #pragma unroll
;     for (int c = 0; c < 4; ++c) { *(unsigned*)(img + (n4 + c) * 68 + (2 * kq) * 2) = cvt_pk_bf16(R.a0[c] * sc, R.b0[c] * sc); *(unsigned*)(img + (n4 + c) * 68 + (2 * kq + 16) * 2) = cvt_pk_bf16(R.a1[c] * sc, R.b1[c] * sc); }
;     asm volatile("" ::: "memory"); __builtin_amdgcn_wave_barrier();
;     const int n = lane >> 1, half = lane & 1; u32x4 w0, w1;
; #pragma unroll
;     for (int j = 0; j < 4; ++j) { w0[j] = *(const unsigned*)(img + n * 68 + half * 32 + j * 4); w1[j] = *(const unsigned*)(img + n * 68 + half * 32 + 16 + j * 4); }
;     const int row = R.c.perm ? R.c.r0 + 128 * ((n >> 3) & 1) + 16 * ((n >> 2) & 1) + 4 * (n >> 4) + (n & 3) : R.c.r0 + 128 * ((n >> 2) & 1) + 4 * (n >> 3) + (n & 3);
;     bf16_t* d = R.c.dst + (size_t)row * R.c.K + R.c.k0 + half * 16;
;     __builtin_nontemporal_store(w0, (u32x4*)d); __builtin_nontemporal_store(w1, (u32x4*)(d + 8));
;     asm volatile("" ::: "memory"); __builtin_amdgcn_wave_barrier();
.LBB0_710:
	s_cmp_eq_u32 s95, 0
	s_cselect_b64 vcc, -1, 0
	s_waitcnt vmcnt(0)
	s_cbranch_scc0 .Lmy_cvs_a
	v_add_u32_e32 v68, v200, v201
	v_cvt_pk_bf16_f32 v67, v154, v158
	v_cvt_pk_bf16_f32 v69, v162, v166
	ds_write2_b32 v68, v67, v69 offset0:0 offset1:8
	v_cvt_pk_bf16_f32 v67, v155, v159
	v_cvt_pk_bf16_f32 v69, v163, v167
	ds_write2_b32 v68, v67, v69 offset0:17 offset1:25
	v_cvt_pk_bf16_f32 v67, v156, v160
	v_cvt_pk_bf16_f32 v69, v164, v168
	ds_write2_b32 v68, v67, v69 offset0:34 offset1:42
	v_cvt_pk_bf16_f32 v67, v157, v161
	v_cvt_pk_bf16_f32 v69, v165, v169
	ds_write2_b32 v68, v67, v69 offset0:51 offset1:59
	v_add_u32_e32 v68, v198, v199
	v_or_b32_e32 v74, v197, v195
	s_branch .Lmy_cvj_a
.Lmy_cvs_a:
	v_cndmask_b32_e64 v66, v181, 1.0, vcc
	v_mul_f32_e32 v67, v66, v154
	v_mul_f32_e32 v68, v66, v158
	v_cvt_pk_bf16_f32 v67, v67, v68
	v_add_u32_e32 v68, v200, v201
	ds_write_b32 v68, v67
	v_mul_f32_e32 v67, v66, v162
	v_mul_f32_e32 v69, v66, v166
	v_cvt_pk_bf16_f32 v67, v67, v69
	ds_write_b32 v68, v67 offset:32
	v_mul_f32_e32 v67, v66, v155
	v_mul_f32_e32 v69, v66, v159
	v_cvt_pk_bf16_f32 v67, v67, v69
	ds_write_b32 v68, v67 offset:68
	v_mul_f32_e32 v67, v66, v163
	v_mul_f32_e32 v69, v66, v167
	v_cvt_pk_bf16_f32 v67, v67, v69
	ds_write_b32 v68, v67 offset:100
	v_mul_f32_e32 v67, v66, v156
	v_mul_f32_e32 v69, v66, v160
	v_cvt_pk_bf16_f32 v67, v67, v69
	ds_write_b32 v68, v67 offset:136
	v_mul_f32_e32 v67, v66, v164
	v_mul_f32_e32 v69, v66, v168
	v_cvt_pk_bf16_f32 v67, v67, v69
	ds_write_b32 v68, v67 offset:168
	v_mul_f32_e32 v67, v66, v157
	v_mul_f32_e32 v69, v66, v161
	v_cvt_pk_bf16_f32 v67, v67, v69
	ds_write_b32 v68, v67 offset:204
	v_mul_f32_e32 v67, v66, v165
	v_mul_f32_e32 v66, v66, v169
	v_cndmask_b32_e32 v74, v196, v197, vcc
	v_cvt_pk_bf16_f32 v66, v67, v66
	ds_write_b32 v68, v66 offset:236
	v_add_u32_e32 v68, v198, v199
	v_or_b32_e32 v74, v74, v195
.Lmy_cvj_a:
	ds_read2_b32 v[66:67], v68 offset1:1
	ds_read2_b32 v[70:71], v68 offset0:4 offset1:5
	ds_read2_b32 v[72:73], v68 offset0:6 offset1:7
	ds_read2_b32 v[68:69], v68 offset0:2 offset1:3
	v_add_u32_e32 v74, s8, v74
	v_mad_i64_i32 v[74:75], s[6:7], v74, s94, 0
	v_lshl_add_u64 v[74:75], v[74:75], 1, v[172:173]
	s_ashr_i32 s11, s10, 31
	v_lshl_add_u64 v[74:75], s[10:11], 1, v[74:75]
	v_lshlrev_b32_e32 v174, 1, v180
	v_lshl_add_u64 v[74:75], v[74:75], 0, v[174:175]
	s_waitcnt lgkmcnt(0)
	global_store_dwordx4 v[74:75], v[66:69], off nt
	global_store_dwordx4 v[74:75], v[70:73], off offset:16 nt
	s_waitcnt vmcnt(2)
	s_cbranch_execz .LBB0_701
	s_branch .LBB0_702
.LBB0_711:
	v_max_f32_e32 v50, v174, v174
	v_max_f32_e32 v249, 0, v50
	v_sub_f32_e32 v50, v98, v249
	v_sub_f32_e32 v51, v99, v249
	v_sub_f32_e32 v52, v100, v249
	v_sub_f32_e32 v53, v101, v249
	v_sub_f32_e32 v54, v102, v249
	v_sub_f32_e32 v55, v103, v249
	v_sub_f32_e32 v56, v104, v249
	v_sub_f32_e32 v57, v105, v249
	v_sub_f32_e32 v58, v106, v249
	v_sub_f32_e32 v59, v107, v249
	v_sub_f32_e32 v60, v108, v249
	v_sub_f32_e32 v61, v109, v249
	v_sub_f32_e32 v62, v110, v249
	v_sub_f32_e32 v63, v111, v249
	v_sub_f32_e32 v64, v112, v249
	v_sub_f32_e32 v65, v113, v249
	v_exp_f32_e64 v202, -v249
	v_add_f32_e32 v203, v209, v249
	v_exp_f32_e32 v50, v50
	v_exp_f32_e32 v51, v51
	v_exp_f32_e32 v52, v52
	v_exp_f32_e32 v53, v53
	v_exp_f32_e32 v54, v54
	v_exp_f32_e32 v55, v55
	v_exp_f32_e32 v56, v56
	v_exp_f32_e32 v57, v57
	v_exp_f32_e32 v58, v58
	v_exp_f32_e32 v59, v59
	v_exp_f32_e32 v60, v60
	v_exp_f32_e32 v61, v61
	v_exp_f32_e32 v62, v62
	v_exp_f32_e32 v63, v63
	v_exp_f32_e32 v64, v64
	v_exp_f32_e32 v65, v65
	v_sub_f32_e32 v81, v81, v249
	v_sub_f32_e32 v80, v80, v249
	v_sub_f32_e32 v79, v79, v249
	v_sub_f32_e32 v78, v78, v249
	v_sub_f32_e32 v77, v77, v249
	v_sub_f32_e32 v76, v76, v249
	v_sub_f32_e32 v75, v75, v249
	v_sub_f32_e32 v74, v74, v249
	v_sub_f32_e32 v73, v73, v249
	v_sub_f32_e32 v72, v72, v249
	v_sub_f32_e32 v71, v71, v249
	v_sub_f32_e32 v70, v70, v249
	v_sub_f32_e32 v69, v69, v249
	v_sub_f32_e32 v68, v68, v249
	v_sub_f32_e32 v67, v67, v249
	v_sub_f32_e32 v66, v66, v249
	s_cbranch_execnz .LBB0_704

; template <bool FIRST> DEVI bool partialSM(f32x16& p0, f32x16& p1, float& m_reg, float& alpha) {
;     float pmax = p0[0];
; #pragma unroll
;     for (int r = 1; r < 16; ++r) pmax = fmaxf(pmax, p0[r]);
; #pragma unroll
;     for (int r = 0; r < 16; ++r) pmax = fmaxf(pmax, p1[r]);
;     { auto rr = __builtin_amdgcn_permlane32_swap(__float_as_uint(pmax), __float_as_uint(pmax), false, false);
;       pmax = fmaxf(__uint_as_float(rr[0]), __uint_as_float(rr[1])); }
;     if (FIRST) { m_reg = pmax; alpha = 1.f;
; #pragma unroll
;         for (int r = 0; r < 16; ++r) { p0[r] = __builtin_amdgcn_exp2f(p0[r] - pmax); p1[r] = p1[r] - pmax; }
;         return false;
;     } else if (__builtin_expect(__all(pmax <= ATT_THR), 1)) { alpha = 1.f;
; #pragma unroll
;         for (int r = 0; r < 16; ++r) p0[r] = __builtin_amdgcn_exp2f(p0[r]);
;         return false;
;     } else { const float d = fmaxf(pmax, 0.f); alpha = __builtin_amdgcn_exp2f(-d); m_reg += d;
; #pragma unroll
;         for (int r = 0; r < 16; ++r) { p0[r] = __builtin_amdgcn_exp2f(p0[r] - d); p1[r] = p1[r] - d; }
;         return true;
;     }
; }
; DEVI void finishSM(f32x16& p0, f32x16& p1, float alpha, float& l_reg, bf16x8& pa0, bf16x8& pa1, bf16x8& pa2, bf16x8& pa3) {
; #pragma unroll
;     for (int r = 0; r < 16; ++r) p1[r] = __builtin_amdgcn_exp2f(p1[r]);
;     f32x2 s2 = (f32x2){p0[0], p0[1]} + (f32x2){p1[0], p1[1]};
; #pragma unroll
;     for (int r = 2; r < 16; r += 2) s2 += (f32x2){p0[r], p0[r + 1]} + (f32x2){p1[r], p1[r + 1]};
;     float ps = s2[0] + s2[1];
;     { auto rr = __builtin_amdgcn_permlane32_swap(__float_as_uint(ps), __float_as_uint(ps), false, false);
;       ps = __uint_as_float(rr[0]) + __uint_as_float(rr[1]); }
;     l_reg = l_reg * alpha + ps;
;     ...
;     PK4(p0, 0, pa0); PK4(p0, 8, pa1); PK4(p1, 0, pa2); PK4(p1, 8, pa3);
;     ...
; }
; DEVI void qkt(f32x16& p0, f32x16& p1, const char* Kb, const bf16x8 (&qr)[6], int r32, int hi, const f32x16& cinit) {
; #pragma unroll
;     for (int d0 = 0; d0 < 6; ++d0) { const int cb = (d0 * 16 + hi * 8) * 2;
;         const bf16x8 k0 = *(const bf16x8*)(Kb + KSWZ(r32, cb)), k1 = *(const bf16x8*)(Kb + KSWZ(32 + r32, cb));
;         p0 = __builtin_amdgcn_mfma_f32_32x32x16_bf16(k0, qr[d0], d0 == 0 ? cinit : p0, 0, 0, 0);
;         p1 = __builtin_amdgcn_mfma_f32_32x32x16_bf16(k1, qr[d0], d0 == 0 ? cinit : p1, 0, 0, 0); }
; }
.LBB0_2260:
	v_add_u32_e32 v174, s98, v205
	v_exp_f32_e32 v66, v66
	v_exp_f32_e32 v67, v67
	s_waitcnt lgkmcnt(1)
	v_mfma_f32_32x32x16_bf16 v[98:113], v[82:85], v[150:153], v[34:49]
	v_add_u32_e32 v82, s98, v184
	v_add_u32_e32 v83, s98, v185
	ds_read_b128 v[210:213], v82 offset:12288
	ds_read_b128 v[214:217], v82 offset:18432
	ds_read_b128 v[218:221], v83 offset:12288
	ds_read_b128 v[222:225], v83 offset:18432
	v_exp_f32_e32 v68, v68
	v_exp_f32_e32 v69, v69
	v_exp_f32_e32 v70, v70
	v_exp_f32_e32 v71, v71
	s_waitcnt lgkmcnt(4)
	v_mfma_f32_32x32x16_bf16 v[82:97], v[124:127], v[150:153], v[34:49]
	ds_read_b128 v[124:127], v174 offset:12288
	ds_read_b128 v[226:229], v174 offset:18432
	v_exp_f32_e32 v72, v72
	v_exp_f32_e32 v73, v73
	v_exp_f32_e32 v74, v74
	v_exp_f32_e32 v75, v75
	v_exp_f32_e32 v76, v76
	v_exp_f32_e32 v77, v77
	s_waitcnt lgkmcnt(5)
	v_mfma_f32_32x32x16_bf16 v[98:113], v[210:213], v[138:141], v[98:113]
	v_add_u32_e32 v174, s98, v206
	v_exp_f32_e32 v78, v78
	v_exp_f32_e32 v79, v79
	ds_read_b128 v[230:233], v174 offset:12288
	ds_read_b128 v[234:237], v174 offset:18432
	v_exp_f32_e32 v80, v80
	v_exp_f32_e32 v81, v81
	v_add_u32_e32 v174, s98, v207
	s_waitcnt lgkmcnt(6)
	v_mfma_f32_32x32x16_bf16 v[82:97], v[214:217], v[138:141], v[82:97]
	v_add_f32_e64 v214, v50, v66
	v_add_f32_e64 v215, v51, v67
	v_add_f32_e64 v216, v52, v68
	v_add_f32_e64 v217, v53, v69
	v_lshl_add_u32 v203, s71, 14, v115
	v_add_f32_e32 v214, v216, v214
	v_add_f32_e32 v215, v217, v215
	v_add_f32_e32 v216, v54, v70
	v_add_f32_e32 v217, v55, v71
	ds_read_b128 v[210:213], v174 offset:12288
	ds_read_b128 v[238:241], v174 offset:18432
	v_add_f32_e32 v214, v216, v214
	v_add_f32_e32 v215, v217, v215
	s_waitcnt lgkmcnt(7)
	v_mfma_f32_32x32x16_bf16 v[98:113], v[218:221], v[134:137], v[98:113]
	v_add_f32_e64 v216, v56, v72
	v_add_f32_e64 v217, v57, v73
	v_cvt_pk_bf16_f32 v50, v50, v51
	v_cvt_pk_bf16_f32 v51, v52, v53
	v_cvt_pk_bf16_f32 v52, v54, v55
	v_cvt_pk_bf16_f32 v53, v56, v57
	v_cvt_pk_bf16_f32 v54, v58, v59
	v_add_f32_e64 v214, v216, v214
	v_add_f32_e64 v215, v217, v215
	s_waitcnt lgkmcnt(6)
	v_mfma_f32_32x32x16_bf16 v[82:97], v[222:225], v[134:137], v[82:97]
	v_add_f32_e64 v216, v58, v74
	v_add_f32_e64 v217, v59, v75
	v_cvt_pk_bf16_f32 v55, v60, v61
	v_cvt_pk_bf16_f32 v56, v62, v63
	v_cvt_pk_bf16_f32 v57, v64, v65
	v_cvt_pk_bf16_f32 v58, v66, v67
	v_cvt_pk_bf16_f32 v59, v68, v69
	v_add_f32_e64 v214, v216, v214
	v_add_f32_e64 v215, v217, v215
	s_waitcnt lgkmcnt(5)
	v_mfma_f32_32x32x16_bf16 v[98:113], v[124:127], v[130:133], v[98:113]
	v_add_f32_e64 v216, v60, v76
	v_add_f32_e64 v217, v61, v77
	v_add_f32_e64 v126, v62, v78
	v_add_f32_e64 v127, v63, v79
	v_add_f32_e64 v124, v216, v214
	v_add_f32_e64 v125, v217, v215
	v_cvt_pk_bf16_f32 v60, v70, v71
	v_cvt_pk_bf16_f32 v61, v72, v73
	v_cvt_pk_bf16_f32 v62, v74, v75
	v_cvt_pk_bf16_f32 v63, v76, v77
	s_waitcnt lgkmcnt(4)
	v_mfma_f32_32x32x16_bf16 v[82:97], v[226:229], v[130:133], v[82:97]
	v_add_f32_e64 v124, v126, v124
	v_add_f32_e64 v125, v127, v125
	v_add_f32_e64 v126, v64, v80
	v_add_f32_e64 v127, v65, v81
	v_cvt_pk_bf16_f32 v64, v78, v79
	v_cvt_pk_bf16_f32 v65, v80, v81
	ds_read_b64_tr_b16 v[66:67], v203 offset:0
	ds_read_b64_tr_b16 v[68:69], v203 offset:0x400
	ds_read_b64_tr_b16 v[70:71], v203 offset:0x800
	s_waitcnt lgkmcnt(6)
	v_mfma_f32_32x32x16_bf16 v[98:113], v[230:233], v[146:149], v[98:113]
	ds_read_b64_tr_b16 v[72:73], v203 offset:0xc00
	ds_read_b64_tr_b16 v[74:75], v203 offset:0x1000
	ds_read_b64_tr_b16 v[76:77], v203 offset:0x1400
	ds_read_b64_tr_b16 v[78:79], v203 offset:0x1800
	ds_read_b64_tr_b16 v[80:81], v203 offset:0x1c00
	v_add_f32_e64 v124, v126, v124
	v_add_f32_e64 v125, v127, v125
	s_waitcnt lgkmcnt(10)
	v_mfma_f32_32x32x16_bf16 v[82:97], v[234:237], v[146:149], v[82:97]
	v_add_f32_e32 v124, v124, v125
	s_nop 0
	v_mov_b32_e32 v125, v124
	s_nop 1
	v_permlane32_swap_b32_e32 v124, v125
	s_waitcnt lgkmcnt(9)
	v_mfma_f32_32x32x16_bf16 v[98:113], v[210:213], v[142:145], v[98:113]
	ds_read_b64_tr_b16 v[210:211], v203 offset:0x200
	ds_read_b64_tr_b16 v[212:213], v203 offset:0x600
	ds_read_b64_tr_b16 v[214:215], v203 offset:0xa00
	ds_read_b64_tr_b16 v[216:217], v203 offset:0xe00
	ds_read_b64_tr_b16 v[218:219], v203 offset:0x1200
	ds_read_b64_tr_b16 v[220:221], v203 offset:0x1600
	ds_read_b64_tr_b16 v[222:223], v203 offset:0x1a00
	s_waitcnt lgkmcnt(15)
	v_mfma_f32_32x32x16_bf16 v[82:97], v[238:241], v[142:145], v[82:97]
	ds_read_b64_tr_b16 v[224:225], v203 offset:0x1e00
	s_waitcnt lgkmcnt(14)
	v_mfma_f32_32x32x16_bf16 v[18:33], v[50:53], v[66:69], v[18:33]
	s_waitcnt lgkmcnt(6)
	v_mfma_f32_32x32x16_bf16 v[2:17], v[50:53], v[210:213], v[2:17]
	s_nop 8
	v_max_f32_e32 v249, v99, v99
	v_max_f32_e32 v250, v98, v98
	v_max_f32_e32 v249, v250, v249
	v_max3_f32 v249, v249, v100, v101
	v_max3_f32 v249, v249, v102, v103
	v_max3_f32 v251, v249, v104, v105
	v_max3_f32 v251, v251, v106, v107
	v_exp_f32_e32 v50, v98
	v_exp_f32_e32 v51, v99
	v_exp_f32_e32 v52, v100
	v_exp_f32_e32 v53, v101
	v_mfma_f32_32x32x16_bf16 v[18:33], v[54:57], v[70:73], v[18:33]
	s_waitcnt lgkmcnt(4)
	v_mfma_f32_32x32x16_bf16 v[2:17], v[54:57], v[214:217], v[2:17]
	v_max3_f32 v251, v251, v108, v109
	v_max3_f32 v251, v251, v110, v111
	v_max3_f32 v251, v251, v112, v113
	v_max3_f32 v251, v251, v82, v83
	v_max3_f32 v251, v251, v84, v85
	v_max3_f32 v251, v251, v86, v87
	v_max3_f32 v251, v251, v88, v89
	v_exp_f32_e32 v54, v102
	v_exp_f32_e32 v55, v103
	v_exp_f32_e32 v56, v104
	v_exp_f32_e32 v57, v105
	v_mfma_f32_32x32x16_bf16 v[18:33], v[58:61], v[74:77], v[18:33]
	s_waitcnt lgkmcnt(2)
	v_mfma_f32_32x32x16_bf16 v[2:17], v[58:61], v[218:221], v[2:17]
	v_max3_f32 v251, v251, v90, v91
	v_max3_f32 v251, v251, v92, v93
	v_max3_f32 v251, v251, v94, v95
	v_max3_f32 v251, v251, v96, v97
	v_mov_b32_e32 v252, v251
	s_nop 1
	v_permlane32_swap_b32_e32 v251, v252
	v_exp_f32_e32 v58, v106
	v_exp_f32_e32 v59, v107
	v_exp_f32_e32 v60, v108
	v_exp_f32_e32 v61, v109
	v_mfma_f32_32x32x16_bf16 v[18:33], v[62:65], v[78:81], v[18:33]
	s_waitcnt lgkmcnt(0)
	v_mfma_f32_32x32x16_bf16 v[2:17], v[62:65], v[222:225], v[2:17]
	v_exp_f32_e32 v62, v110
	v_exp_f32_e32 v63, v111
	v_exp_f32_e32 v64, v112
	v_exp_f32_e32 v65, v113
	v_max_f32_e32 v252, v252, v252
	v_max_f32_e32 v251, v251, v251
	v_max_f32_e32 v126, v251, v252
	v_cmp_ge_f32_e32 vcc, s80, v126
	s_cmp_lg_u64 vcc, exec
	s_cselect_b64 s[6:7], -1, 0
	s_cbranch_scc1 .LBB0_2269
	v_mov_b32_e32 v209, 1.0
	v_mov_b32_e32 v210, v204
	s_branch .LBB0_2263

; #define VM0() asm volatile("s_waitcnt vmcnt(0)" ::: "memory")
; DEVI void attn_unit8(const Params& p, char* smem, int unit, int l, int& cvs  , CvRun& crun) {
;     ...
;         if (cvr.live) asm volatile("s_waitcnt vmcnt(2)" ::: "memory"); else VM0();
;         __syncthreads();
;         if (T + 2 < NTILE) B_DMA(T + 2, s2);
;         qkt(pA0, pA1, K_lds + s1 * 24576, qr, r32, hi, cinit);
.LBB0_2266:
	s_mul_i32 s98, s61, 0x6000
	s_add_i32 s98, s96, s98
	s_lshl_b32 s99, s61, 14
	s_add_i32 s99, s97, s99
	s_mul_i32 s6, s2, 0x6000
	s_add_i32 s6, s6, 0
	v_add_u32_e32 v249, s6, v129
	v_lshl_add_u64 v[250:251], v[118:119], 0, s[12:13]
	s_mov_b32 m0, s98
	s_barrier
; template <bool FIRST> DEVI bool partialSM(f32x16& p0, f32x16& p1, float& m_reg, float& alpha) {
;     float pmax = p0[0];
; #pragma unroll
;     for (int r = 1; r < 16; ++r) pmax = fmaxf(pmax, p0[r]);
; #pragma unroll
;     for (int r = 0; r < 16; ++r) pmax = fmaxf(pmax, p1[r]);
;     { auto rr = __builtin_amdgcn_permlane32_swap(__float_as_uint(pmax), __float_as_uint(pmax), false, false);
;       pmax = fmaxf(__uint_as_float(rr[0]), __uint_as_float(rr[1])); }
;     if (FIRST) { m_reg = pmax; alpha = 1.f;
; #pragma unroll
;         for (int r = 0; r < 16; ++r) { p0[r] = __builtin_amdgcn_exp2f(p0[r] - pmax); p1[r] = p1[r] - pmax; }
;         return false;
;     } else if (__builtin_expect(__all(pmax <= ATT_THR), 1)) { alpha = 1.f;
; #pragma unroll
;         for (int r = 0; r < 16; ++r) p0[r] = __builtin_amdgcn_exp2f(p0[r]);
;         return false;
;     } else { const float d = fmaxf(pmax, 0.f); alpha = __builtin_amdgcn_exp2f(-d); m_reg += d;
; #pragma unroll
;         for (int r = 0; r < 16; ++r) { p0[r] = __builtin_amdgcn_exp2f(p0[r] - d); p1[r] = p1[r] - d; }
;         return true;
;     }
; }
; DEVI void finishSM(f32x16& p0, f32x16& p1, float alpha, float& l_reg, bf16x8& pa0, bf16x8& pa1, bf16x8& pa2, bf16x8& pa3) {
; #pragma unroll
;     for (int r = 0; r < 16; ++r) p1[r] = __builtin_amdgcn_exp2f(p1[r]);
;     f32x2 s2 = (f32x2){p0[0], p0[1]} + (f32x2){p1[0], p1[1]};
; #pragma unroll
;     for (int r = 2; r < 16; r += 2) s2 += (f32x2){p0[r], p0[r + 1]} + (f32x2){p1[r], p1[r + 1]};
;     float ps = s2[0] + s2[1];
;     { auto rr = __builtin_amdgcn_permlane32_swap(__float_as_uint(ps), __float_as_uint(ps), false, false);
;       ps = __uint_as_float(rr[0]) + __uint_as_float(rr[1]); }
;     l_reg = l_reg * alpha + ps;
;     ...
;     PK4(p0, 0, pa0); PK4(p0, 8, pa1); PK4(p1, 0, pa2); PK4(p1, 8, pa3);
;     ...
; }
; DEVI void qkt(f32x16& p0, f32x16& p1, const char* Kb, const bf16x8 (&qr)[6], int r32, int hi, const f32x16& cinit) {
; #pragma unroll
;     for (int d0 = 0; d0 < 6; ++d0) { const int cb = (d0 * 16 + hi * 8) * 2;
;         const bf16x8 k0 = *(const bf16x8*)(Kb + KSWZ(r32, cb)), k1 = *(const bf16x8*)(Kb + KSWZ(32 + r32, cb));
;         p0 = __builtin_amdgcn_mfma_f32_32x32x16_bf16(k0, qr[d0], d0 == 0 ? cinit : p0, 0, 0, 0);
;         p1 = __builtin_amdgcn_mfma_f32_32x32x16_bf16(k1, qr[d0], d0 == 0 ? cinit : p1, 0, 0, 0); }
; }
	ds_read_b128 v[234:237], v249
	ds_read_b128 v[212:215], v249 offset:6144
	global_load_lds_dwordx4 v[250:251], off
	v_exp_f32_e32 v82, v82
	s_waitcnt lgkmcnt(1)
	v_mfma_f32_32x32x16_bf16 v[98:113], v[234:237], v[150:153], v[34:49]
	v_add_u32_e32 v126, s6, v184
	v_lshl_add_u64 v[250:251], v[120:121], 0, s[12:13]
	s_add_i32 m0, s98, 0x2000
	v_exp_f32_e32 v83, v83
	v_exp_f32_e32 v84, v84
	global_load_lds_dwordx4 v[250:251], off
	v_exp_f32_e32 v85, v85
	v_exp_f32_e32 v86, v86
	v_exp_f32_e32 v87, v87
	v_exp_f32_e32 v88, v88
	s_waitcnt lgkmcnt(0)
	v_mfma_f32_32x32x16_bf16 v[66:81], v[212:215], v[150:153], v[34:49]
	ds_read_b128 v[212:215], v126
	ds_read_b128 v[216:219], v126 offset:6144
	v_add_u32_e32 v126, s6, v185
	v_lshl_add_u64 v[250:251], v[122:123], 0, s[12:13]
	s_add_i32 m0, s98, 0x4000
	v_exp_f32_e32 v89, v89
	v_exp_f32_e32 v90, v90
	global_load_lds_dwordx4 v[250:251], off
	v_exp_f32_e32 v91, v91
	v_exp_f32_e32 v92, v92
	v_exp_f32_e32 v93, v93
	s_waitcnt lgkmcnt(1)
	v_mfma_f32_32x32x16_bf16 v[98:113], v[212:215], v[138:141], v[98:113]
	s_mov_b32 m0, s99
	v_exp_f32_e32 v94, v94
	v_exp_f32_e32 v95, v95
	v_lshl_add_u64 v[250:251], v[116:117], 0, s[40:41]
	global_load_lds_dwordx4 v[116:117], off
	s_add_i32 m0, s99, 0x2000
	v_exp_f32_e32 v96, v96
	v_exp_f32_e32 v97, v97
	v_add_u32_e32 v174, 0x2000, v203
	global_load_lds_dwordx4 v[250:251], off
	s_waitcnt lgkmcnt(0)
	v_mfma_f32_32x32x16_bf16 v[66:81], v[216:219], v[138:141], v[66:81]
	ds_read_b128 v[212:215], v126
	ds_read_b128 v[216:219], v126 offset:6144
	v_add_u32_e32 v126, s6, v205
	s_waitcnt lgkmcnt(1)
	v_mfma_f32_32x32x16_bf16 v[98:113], v[212:215], v[134:137], v[98:113]
	ds_read_b128 v[212:215], v126
	ds_read_b128 v[220:223], v126 offset:6144
	v_add_u32_e32 v126, s6, v206
	s_waitcnt lgkmcnt(2)
	v_mfma_f32_32x32x16_bf16 v[66:81], v[216:219], v[134:137], v[66:81]
	ds_read_b128 v[216:219], v126
	ds_read_b128 v[224:227], v126 offset:6144
	v_add_u32_e32 v126, s6, v207
	ds_read_b128 v[228:231], v126
	ds_read_b128 v[232:235], v126 offset:6144
	v_add_f32_e32 v126, v50, v82
	v_add_f32_e32 v127, v51, v83
	v_cvt_pk_bf16_f32 v50, v50, v51
	v_cvt_pk_bf16_f32 v51, v52, v53
	s_waitcnt lgkmcnt(5)
	v_mfma_f32_32x32x16_bf16 v[98:113], v[212:215], v[130:133], v[98:113]
	v_add_f32_e64 v212, v52, v84
	v_add_f32_e64 v213, v53, v85
	v_cvt_pk_bf16_f32 v52, v54, v55
	v_cvt_pk_bf16_f32 v53, v56, v57
	v_add_f32_e64 v126, v212, v126
	v_add_f32_e64 v127, v213, v127
	v_add_f32_e64 v212, v54, v86
	v_add_f32_e64 v213, v55, v87
	v_cvt_pk_bf16_f32 v54, v58, v59
	s_waitcnt lgkmcnt(4)
	v_mfma_f32_32x32x16_bf16 v[66:81], v[220:223], v[130:133], v[66:81]
	v_add_f32_e64 v126, v212, v126
	v_add_f32_e64 v127, v213, v127
	v_add_f32_e64 v212, v56, v88
	v_add_f32_e64 v213, v57, v89
	v_cvt_pk_bf16_f32 v55, v60, v61
	v_cvt_pk_bf16_f32 v56, v62, v63
	v_cvt_pk_bf16_f32 v57, v64, v65
	v_add_f32_e64 v126, v212, v126
	v_add_f32_e64 v127, v213, v127
	v_add_f32_e32 v212, v58, v90
	v_add_f32_e32 v213, v59, v91
	v_cvt_pk_bf16_f32 v58, v82, v83
	v_cvt_pk_bf16_f32 v59, v84, v85
	s_waitcnt lgkmcnt(3)
	v_mfma_f32_32x32x16_bf16 v[98:113], v[216:219], v[146:149], v[98:113]
	v_add_f32_e64 v126, v212, v126
	v_add_f32_e64 v127, v213, v127
	v_add_f32_e64 v212, v60, v92
	v_add_f32_e64 v213, v61, v93
	v_cvt_pk_bf16_f32 v60, v86, v87
	v_cvt_pk_bf16_f32 v61, v88, v89
	v_add_f32_e64 v126, v212, v126
	v_add_f32_e64 v127, v213, v127
	v_add_f32_e32 v212, v62, v94
	v_add_f32_e32 v213, v63, v95
	v_cvt_pk_bf16_f32 v62, v90, v91
	v_cvt_pk_bf16_f32 v63, v92, v93
	s_waitcnt lgkmcnt(2)
	v_mfma_f32_32x32x16_bf16 v[66:81], v[224:227], v[146:149], v[66:81]
	v_add_f32_e64 v126, v212, v126
	v_add_f32_e64 v127, v213, v127
	v_add_f32_e64 v212, v64, v96
	v_add_f32_e64 v213, v65, v97
	v_cvt_pk_bf16_f32 v64, v94, v95
	v_cvt_pk_bf16_f32 v65, v96, v97
	ds_read_b64_tr_b16 v[154:155], v174 offset:0
	ds_read_b64_tr_b16 v[156:157], v174 offset:0x400
	ds_read_b64_tr_b16 v[158:159], v174 offset:0x800
	ds_read_b64_tr_b16 v[160:161], v174 offset:0xc00
	ds_read_b64_tr_b16 v[162:163], v174 offset:0x1000
	ds_read_b64_tr_b16 v[164:165], v174 offset:0x1400
	ds_read_b64_tr_b16 v[166:167], v174 offset:0x1800
	ds_read_b64_tr_b16 v[168:169], v174 offset:0x1c00
	v_add_f32_e64 v126, v212, v126
	v_add_f32_e64 v127, v213, v127
	ds_read_b64_tr_b16 v[212:213], v174 offset:0x200
	ds_read_b64_tr_b16 v[214:215], v174 offset:0x600
	ds_read_b64_tr_b16 v[216:217], v174 offset:0xa00
	s_waitcnt lgkmcnt(12)
	v_mfma_f32_32x32x16_bf16 v[98:113], v[228:231], v[142:145], v[98:113]
	ds_read_b64_tr_b16 v[218:219], v174 offset:0xe00
	ds_read_b64_tr_b16 v[220:221], v174 offset:0x1200
	ds_read_b64_tr_b16 v[222:223], v174 offset:0x1600
	ds_read_b64_tr_b16 v[224:225], v174 offset:0x1a00
	ds_read_b64_tr_b16 v[226:227], v174 offset:0x1e00
	v_add_f32_e32 v126, v126, v127
	s_waitcnt lgkmcnt(15)
	v_mfma_f32_32x32x16_bf16 v[66:81], v[232:235], v[142:145], v[66:81]
	v_mov_b32_e32 v127, v126
	s_nop 1
	v_permlane32_swap_b32_e32 v126, v127
	s_waitcnt lgkmcnt(14)
	v_mfma_f32_32x32x16_bf16 v[18:33], v[50:53], v[154:157], v[18:33]
	s_waitcnt lgkmcnt(6)
	v_mfma_f32_32x32x16_bf16 v[2:17], v[50:53], v[212:215], v[2:17]
	s_nop 4
	v_max_f32_e32 v249, v99, v99
	v_max_f32_e32 v250, v98, v98
	v_max_f32_e32 v249, v250, v249
	v_max3_f32 v249, v249, v100, v101
	v_max3_f32 v249, v249, v102, v103
	v_max3_f32 v251, v249, v104, v105
	v_max3_f32 v251, v251, v106, v107
	v_exp_f32_e32 v50, v98
	v_exp_f32_e32 v51, v99
	v_exp_f32_e32 v52, v100
	v_exp_f32_e32 v53, v101
	v_mfma_f32_32x32x16_bf16 v[18:33], v[54:57], v[158:161], v[18:33]
	s_waitcnt lgkmcnt(4)
	v_mfma_f32_32x32x16_bf16 v[2:17], v[54:57], v[216:219], v[2:17]
	v_max3_f32 v251, v251, v108, v109
	v_max3_f32 v251, v251, v110, v111
	v_max3_f32 v251, v251, v112, v113
	v_max3_f32 v251, v251, v66, v67
	v_max3_f32 v251, v251, v68, v69
	v_max3_f32 v251, v251, v70, v71
	v_max3_f32 v251, v251, v72, v73
	v_exp_f32_e32 v54, v102
	v_exp_f32_e32 v55, v103
	v_exp_f32_e32 v56, v104
	v_exp_f32_e32 v57, v105
	v_mfma_f32_32x32x16_bf16 v[18:33], v[58:61], v[162:165], v[18:33]
	s_waitcnt lgkmcnt(2)
	v_mfma_f32_32x32x16_bf16 v[2:17], v[58:61], v[220:223], v[2:17]
	v_max3_f32 v251, v251, v74, v75
	v_max3_f32 v251, v251, v76, v77
	v_max3_f32 v251, v251, v78, v79
	v_max3_f32 v251, v251, v80, v81
	v_mov_b32_e32 v252, v251
	s_nop 1
	v_permlane32_swap_b32_e32 v251, v252
	v_exp_f32_e32 v58, v106
	v_exp_f32_e32 v59, v107
	v_exp_f32_e32 v60, v108
	v_exp_f32_e32 v61, v109
	v_mfma_f32_32x32x16_bf16 v[18:33], v[62:65], v[166:169], v[18:33]
	s_waitcnt lgkmcnt(0)
	v_mfma_f32_32x32x16_bf16 v[2:17], v[62:65], v[224:227], v[2:17]
	v_exp_f32_e32 v62, v110
	v_exp_f32_e32 v63, v111
	v_exp_f32_e32 v64, v112
	v_exp_f32_e32 v65, v113
	v_max_f32_e32 v252, v252, v252
	v_max_f32_e32 v251, v251, v251
	v_max_f32_e32 v174, v251, v252
	v_cmp_ge_f32_e32 vcc, s80, v174
	s_cmp_lg_u64 vcc, exec
	s_cselect_b64 s[6:7], -1, 0
	s_cbranch_scc1 .LBB0_2275
	v_mov_b32_e32 v203, 1.0
	v_mov_b32_e32 v204, v210
	s_branch .LBB0_2280

; template <bool FIRST> DEVI bool partialSM(f32x16& p0, f32x16& p1, float& m_reg, float& alpha) {
;     ...
;     } else { const float d = fmaxf(pmax, 0.f); alpha = __builtin_amdgcn_exp2f(-d); m_reg += d;
; #pragma unroll
;         for (int r = 0; r < 16; ++r) { p0[r] = __builtin_amdgcn_exp2f(p0[r] - d); p1[r] = p1[r] - d; }
;         return true;
;     }
.LBB0_2269:
	v_max_f32_e32 v50, v126, v126
	v_max_f32_e32 v66, 0, v50
	v_sub_f32_e32 v50, v98, v66
	v_sub_f32_e32 v51, v99, v66
	v_sub_f32_e32 v52, v100, v66
	v_sub_f32_e32 v53, v101, v66
	v_sub_f32_e32 v54, v102, v66
	v_sub_f32_e32 v55, v103, v66
	v_sub_f32_e32 v56, v104, v66
	v_sub_f32_e32 v57, v105, v66
	v_sub_f32_e32 v58, v106, v66
	v_sub_f32_e32 v59, v107, v66
	v_sub_f32_e32 v60, v108, v66
	v_sub_f32_e32 v61, v109, v66
	v_sub_f32_e32 v62, v110, v66
	v_sub_f32_e32 v63, v111, v66
	v_sub_f32_e32 v64, v112, v66
	v_sub_f32_e32 v65, v113, v66
	v_exp_f32_e64 v209, -v66
	v_add_f32_e32 v210, v204, v66
	v_exp_f32_e32 v50, v50
	v_exp_f32_e32 v51, v51
	v_exp_f32_e32 v52, v52
	v_exp_f32_e32 v53, v53
	v_exp_f32_e32 v54, v54
	v_exp_f32_e32 v55, v55
	v_exp_f32_e32 v56, v56
	v_exp_f32_e32 v57, v57
	v_exp_f32_e32 v58, v58
	v_exp_f32_e32 v59, v59
	v_exp_f32_e32 v60, v60
	v_exp_f32_e32 v61, v61
	v_exp_f32_e32 v62, v62
	v_exp_f32_e32 v63, v63
	v_exp_f32_e32 v64, v64
	v_exp_f32_e32 v65, v65
	v_sub_f32_e32 v97, v97, v66
	v_sub_f32_e32 v96, v96, v66
	v_sub_f32_e32 v95, v95, v66
	v_sub_f32_e32 v94, v94, v66
	v_sub_f32_e32 v93, v93, v66
	v_sub_f32_e32 v92, v92, v66
	v_sub_f32_e32 v91, v91, v66
	v_sub_f32_e32 v90, v90, v66
	v_sub_f32_e32 v89, v89, v66
	v_sub_f32_e32 v88, v88, v66
	v_sub_f32_e32 v87, v87, v66
	v_sub_f32_e32 v86, v86, v66
	v_sub_f32_e32 v85, v85, v66
	v_sub_f32_e32 v84, v84, v66
	v_sub_f32_e32 v83, v83, v66
	v_sub_f32_e32 v82, v82, v66
	s_cbranch_execnz .LBB0_2262

; DEVI unsigned cvt_pk_bf16(float lo, float hi) { unsigned r; asm volatile("v_cvt_pk_bf16_f32 %0, %1, %2" : "=v"(r) : "v"(lo), "v"(hi)); return r; }
; DEVI void cv_finish(char* img  , int lane, const CvRegs& R) {
;     if (!R.live) return;
;     const int n4 = (lane & 7) * 4, kq = lane >> 3;
;     const float sc = R.c.perm ? 16.f : 1.f;
; #pragma unroll
;     for (int c = 0; c < 4; ++c) { *(unsigned*)(img + (n4 + c) * 68 + (2 * kq) * 2) = cvt_pk_bf16(R.a0[c] * sc, R.b0[c] * sc); *(unsigned*)(img + (n4 + c) * 68 + (2 * kq + 16) * 2) = cvt_pk_bf16(R.a1[c] * sc, R.b1[c] * sc); }
;     asm volatile("" ::: "memory"); __builtin_amdgcn_wave_barrier();
;     const int n = lane >> 1, half = lane & 1; u32x4 w0, w1;
.LBB0_2274:
	s_cmp_eq_u32 s95, 0
	s_cselect_b64 vcc, -1, 0
	s_waitcnt vmcnt(0)
	s_cbranch_scc0 .Lmy_cvs_b
	v_add_u32_e32 v68, v201, v202
	v_cvt_pk_bf16_f32 v67, v154, v158
	v_cvt_pk_bf16_f32 v69, v162, v166
	ds_write2_b32 v68, v67, v69 offset0:0 offset1:8
	v_cvt_pk_bf16_f32 v67, v155, v159
	v_cvt_pk_bf16_f32 v69, v163, v167
	ds_write2_b32 v68, v67, v69 offset0:17 offset1:25
	v_cvt_pk_bf16_f32 v67, v156, v160
	v_cvt_pk_bf16_f32 v69, v164, v168
	ds_write2_b32 v68, v67, v69 offset0:34 offset1:42
	v_cvt_pk_bf16_f32 v67, v157, v161
	v_cvt_pk_bf16_f32 v69, v165, v169
	ds_write2_b32 v68, v67, v69 offset0:51 offset1:59
	v_add_u32_e32 v68, v199, v200
	v_or_b32_e32 v74, v198, v196
	s_branch .Lmy_cvj_b
.Lmy_cvs_b:
	v_cndmask_b32_e64 v66, v186, 1.0, vcc
	v_mul_f32_e32 v67, v66, v154
	v_mul_f32_e32 v68, v66, v158
	v_cvt_pk_bf16_f32 v67, v67, v68
	v_add_u32_e32 v68, v201, v202
	ds_write_b32 v68, v67
	v_mul_f32_e32 v67, v66, v162
	v_mul_f32_e32 v69, v66, v166
	v_cvt_pk_bf16_f32 v67, v67, v69
	ds_write_b32 v68, v67 offset:32
	v_mul_f32_e32 v67, v66, v155
	v_mul_f32_e32 v69, v66, v159
	v_cvt_pk_bf16_f32 v67, v67, v69
	ds_write_b32 v68, v67 offset:68
	v_mul_f32_e32 v67, v66, v163
	v_mul_f32_e32 v69, v66, v167
	v_cvt_pk_bf16_f32 v67, v67, v69
	ds_write_b32 v68, v67 offset:100
	v_mul_f32_e32 v67, v66, v156
	v_mul_f32_e32 v69, v66, v160
	v_cvt_pk_bf16_f32 v67, v67, v69
	ds_write_b32 v68, v67 offset:136
	v_mul_f32_e32 v67, v66, v164
	v_mul_f32_e32 v69, v66, v168
	v_cvt_pk_bf16_f32 v67, v67, v69
	ds_write_b32 v68, v67 offset:168
	v_mul_f32_e32 v67, v66, v157
	v_mul_f32_e32 v69, v66, v161
	v_cvt_pk_bf16_f32 v67, v67, v69
	ds_write_b32 v68, v67 offset:204
	v_mul_f32_e32 v67, v66, v165
	v_mul_f32_e32 v66, v66, v169
	v_cndmask_b32_e32 v74, v197, v198, vcc
	v_cvt_pk_bf16_f32 v66, v67, v66
	ds_write_b32 v68, v66 offset:236
	v_add_u32_e32 v68, v199, v200
	v_or_b32_e32 v74, v74, v196

; template <bool FIRST> DEVI bool partialSM(f32x16& p0, f32x16& p1, float& m_reg, float& alpha) {
;     ...
;     } else { const float d = fmaxf(pmax, 0.f); alpha = __builtin_amdgcn_exp2f(-d); m_reg += d;
; #pragma unroll
;         for (int r = 0; r < 16; ++r) { p0[r] = __builtin_amdgcn_exp2f(p0[r] - d); p1[r] = p1[r] - d; }
;         return true;
;     }
.LBB0_2275:
	v_max_f32_e32 v50, v174, v174
	v_max_f32_e32 v249, 0, v50
	v_sub_f32_e32 v50, v98, v249
	v_sub_f32_e32 v51, v99, v249
	v_sub_f32_e32 v52, v100, v249
	v_sub_f32_e32 v53, v101, v249
	v_sub_f32_e32 v54, v102, v249
	v_sub_f32_e32 v55, v103, v249
	v_sub_f32_e32 v56, v104, v249
	v_sub_f32_e32 v57, v105, v249
	v_sub_f32_e32 v58, v106, v249
	v_sub_f32_e32 v59, v107, v249
	v_sub_f32_e32 v60, v108, v249
	v_sub_f32_e32 v61, v109, v249
	v_sub_f32_e32 v62, v110, v249
	v_sub_f32_e32 v63, v111, v249
	v_sub_f32_e32 v64, v112, v249
	v_sub_f32_e32 v65, v113, v249
	v_exp_f32_e64 v203, -v249
	v_add_f32_e32 v204, v210, v249
	v_exp_f32_e32 v50, v50
	v_exp_f32_e32 v51, v51
	v_exp_f32_e32 v52, v52
	v_exp_f32_e32 v53, v53
	v_exp_f32_e32 v54, v54
	v_exp_f32_e32 v55, v55
	v_exp_f32_e32 v56, v56
	v_exp_f32_e32 v57, v57
	v_exp_f32_e32 v58, v58
	v_exp_f32_e32 v59, v59
	v_exp_f32_e32 v60, v60
	v_exp_f32_e32 v61, v61
	v_exp_f32_e32 v62, v62
	v_exp_f32_e32 v63, v63
	v_exp_f32_e32 v64, v64
	v_exp_f32_e32 v65, v65
	v_sub_f32_e32 v81, v81, v249
	v_sub_f32_e32 v80, v80, v249
	v_sub_f32_e32 v79, v79, v249
	v_sub_f32_e32 v78, v78, v249
	v_sub_f32_e32 v77, v77, v249
	v_sub_f32_e32 v76, v76, v249
	v_sub_f32_e32 v75, v75, v249
	v_sub_f32_e32 v74, v74, v249
	v_sub_f32_e32 v73, v73, v249
	v_sub_f32_e32 v72, v72, v249
	v_sub_f32_e32 v71, v71, v249
	v_sub_f32_e32 v70, v70, v249
	v_sub_f32_e32 v69, v69, v249
	v_sub_f32_e32 v68, v68, v249
	v_sub_f32_e32 v67, v67, v249
	v_sub_f32_e32 v66, v66, v249
	s_cbranch_execnz .LBB0_2268
